# router_c0 (router constant term, one wave on the critical path of the norm phases): 16 sequential wave reductions interleaved into one butterfly
# speedup vs baseline: 1.0015x; 1.0015x over previous
.LBB0_88:
	s_or_b64 exec, exec, s[8:9]
	s_load_dwordx2 s[0:1], s[6:7], 0x1b8
	v_cmp_eq_u32_e32 vcc, 0, v0
	v_lshlrev_b32_e32 v34, 2, v144
	v_xor_b32_e32 v35, 0x4, v34
	ds_bpermute_b32 v18, v35, v16
	ds_bpermute_b32 v19, v35, v17
	ds_bpermute_b32 v20, v35, v14
	ds_bpermute_b32 v21, v35, v15
	ds_bpermute_b32 v22, v35, v12
	ds_bpermute_b32 v23, v35, v13
	ds_bpermute_b32 v24, v35, v10
	ds_bpermute_b32 v25, v35, v11
	s_waitcnt lgkmcnt(0)
	v_add_f32_e32 v16, v16, v18
	v_add_f32_e32 v17, v17, v19
	v_add_f32_e32 v14, v14, v20
	v_add_f32_e32 v15, v15, v21
	v_add_f32_e32 v12, v12, v22
	v_add_f32_e32 v13, v13, v23
	v_add_f32_e32 v10, v10, v24
	v_add_f32_e32 v11, v11, v25
	ds_bpermute_b32 v26, v35, v8
	ds_bpermute_b32 v27, v35, v9
	ds_bpermute_b32 v28, v35, v6
	ds_bpermute_b32 v29, v35, v7
	ds_bpermute_b32 v30, v35, v4
	ds_bpermute_b32 v31, v35, v5
	ds_bpermute_b32 v32, v35, v2
	ds_bpermute_b32 v33, v35, v3
	s_waitcnt lgkmcnt(0)
	v_add_f32_e32 v8, v8, v26
	v_add_f32_e32 v9, v9, v27
	v_add_f32_e32 v6, v6, v28
	v_add_f32_e32 v7, v7, v29
	v_add_f32_e32 v4, v4, v30
	v_add_f32_e32 v5, v5, v31
	v_add_f32_e32 v2, v2, v32
	v_add_f32_e32 v3, v3, v33
	v_xor_b32_e32 v35, 0x8, v34
	ds_bpermute_b32 v18, v35, v16
	ds_bpermute_b32 v19, v35, v17
	ds_bpermute_b32 v20, v35, v14
	ds_bpermute_b32 v21, v35, v15
	ds_bpermute_b32 v22, v35, v12
	ds_bpermute_b32 v23, v35, v13
	ds_bpermute_b32 v24, v35, v10
	ds_bpermute_b32 v25, v35, v11
	s_waitcnt lgkmcnt(0)
	v_add_f32_e32 v16, v16, v18
	v_add_f32_e32 v17, v17, v19
	v_add_f32_e32 v14, v14, v20
	v_add_f32_e32 v15, v15, v21
	v_add_f32_e32 v12, v12, v22
	v_add_f32_e32 v13, v13, v23
	v_add_f32_e32 v10, v10, v24
	v_add_f32_e32 v11, v11, v25
	ds_bpermute_b32 v26, v35, v8
	ds_bpermute_b32 v27, v35, v9
	ds_bpermute_b32 v28, v35, v6
	ds_bpermute_b32 v29, v35, v7
	ds_bpermute_b32 v30, v35, v4
	ds_bpermute_b32 v31, v35, v5
	ds_bpermute_b32 v32, v35, v2
	ds_bpermute_b32 v33, v35, v3
	s_waitcnt lgkmcnt(0)
	v_add_f32_e32 v8, v8, v26
	v_add_f32_e32 v9, v9, v27
	v_add_f32_e32 v6, v6, v28
	v_add_f32_e32 v7, v7, v29
	v_add_f32_e32 v4, v4, v30
	v_add_f32_e32 v5, v5, v31
	v_add_f32_e32 v2, v2, v32
	v_add_f32_e32 v3, v3, v33
	v_xor_b32_e32 v35, 0x10, v34
	ds_bpermute_b32 v18, v35, v16
	ds_bpermute_b32 v19, v35, v17
	ds_bpermute_b32 v20, v35, v14
	ds_bpermute_b32 v21, v35, v15
	ds_bpermute_b32 v22, v35, v12
	ds_bpermute_b32 v23, v35, v13
	ds_bpermute_b32 v24, v35, v10
	ds_bpermute_b32 v25, v35, v11
	s_waitcnt lgkmcnt(0)
	v_add_f32_e32 v16, v16, v18
	v_add_f32_e32 v17, v17, v19
	v_add_f32_e32 v14, v14, v20
	v_add_f32_e32 v15, v15, v21
	v_add_f32_e32 v12, v12, v22
	v_add_f32_e32 v13, v13, v23
	v_add_f32_e32 v10, v10, v24
	v_add_f32_e32 v11, v11, v25
	ds_bpermute_b32 v26, v35, v8
	ds_bpermute_b32 v27, v35, v9
	ds_bpermute_b32 v28, v35, v6
	ds_bpermute_b32 v29, v35, v7
	ds_bpermute_b32 v30, v35, v4
	ds_bpermute_b32 v31, v35, v5
	ds_bpermute_b32 v32, v35, v2
	ds_bpermute_b32 v33, v35, v3
	s_waitcnt lgkmcnt(0)
	v_add_f32_e32 v8, v8, v26
	v_add_f32_e32 v9, v9, v27
	v_add_f32_e32 v6, v6, v28
	v_add_f32_e32 v7, v7, v29
	v_add_f32_e32 v4, v4, v30
	v_add_f32_e32 v5, v5, v31
	v_add_f32_e32 v2, v2, v32
	v_add_f32_e32 v3, v3, v33
	v_xor_b32_e32 v35, 0x20, v34
	ds_bpermute_b32 v18, v35, v16
	ds_bpermute_b32 v19, v35, v17
	ds_bpermute_b32 v20, v35, v14
	ds_bpermute_b32 v21, v35, v15
	ds_bpermute_b32 v22, v35, v12
	ds_bpermute_b32 v23, v35, v13
	ds_bpermute_b32 v24, v35, v10
	ds_bpermute_b32 v25, v35, v11
	s_waitcnt lgkmcnt(0)
	v_add_f32_e32 v16, v16, v18
	v_add_f32_e32 v17, v17, v19
	v_add_f32_e32 v14, v14, v20
	v_add_f32_e32 v15, v15, v21
	v_add_f32_e32 v12, v12, v22
	v_add_f32_e32 v13, v13, v23
	v_add_f32_e32 v10, v10, v24
	v_add_f32_e32 v11, v11, v25
	ds_bpermute_b32 v26, v35, v8
	ds_bpermute_b32 v27, v35, v9
	ds_bpermute_b32 v28, v35, v6
	ds_bpermute_b32 v29, v35, v7
	ds_bpermute_b32 v30, v35, v4
	ds_bpermute_b32 v31, v35, v5
	ds_bpermute_b32 v32, v35, v2
	ds_bpermute_b32 v33, v35, v3
	s_waitcnt lgkmcnt(0)
	v_add_f32_e32 v8, v8, v26
	v_add_f32_e32 v9, v9, v27
	v_add_f32_e32 v6, v6, v28
	v_add_f32_e32 v7, v7, v29
	v_add_f32_e32 v4, v4, v30
	v_add_f32_e32 v5, v5, v31
	v_add_f32_e32 v2, v2, v32
	v_add_f32_e32 v3, v3, v33
	v_xor_b32_e32 v35, 0x40, v34
	ds_bpermute_b32 v18, v35, v16
	ds_bpermute_b32 v19, v35, v17
	ds_bpermute_b32 v20, v35, v14
	ds_bpermute_b32 v21, v35, v15
	ds_bpermute_b32 v22, v35, v12
	ds_bpermute_b32 v23, v35, v13
	ds_bpermute_b32 v24, v35, v10
	ds_bpermute_b32 v25, v35, v11
	s_waitcnt lgkmcnt(0)
	v_add_f32_e32 v16, v16, v18
	v_add_f32_e32 v17, v17, v19
	v_add_f32_e32 v14, v14, v20
	v_add_f32_e32 v15, v15, v21
	v_add_f32_e32 v12, v12, v22
	v_add_f32_e32 v13, v13, v23
	v_add_f32_e32 v10, v10, v24
	v_add_f32_e32 v11, v11, v25
	ds_bpermute_b32 v26, v35, v8
	ds_bpermute_b32 v27, v35, v9
	ds_bpermute_b32 v28, v35, v6
	ds_bpermute_b32 v29, v35, v7
	ds_bpermute_b32 v30, v35, v4
	ds_bpermute_b32 v31, v35, v5
	ds_bpermute_b32 v32, v35, v2
	ds_bpermute_b32 v33, v35, v3
	s_waitcnt lgkmcnt(0)
	v_add_f32_e32 v8, v8, v26
	v_add_f32_e32 v9, v9, v27
	v_add_f32_e32 v6, v6, v28
	v_add_f32_e32 v7, v7, v29
	v_add_f32_e32 v4, v4, v30
	v_add_f32_e32 v5, v5, v31
	v_add_f32_e32 v2, v2, v32
	v_add_f32_e32 v3, v3, v33
	v_xor_b32_e32 v35, 0x80, v34
	ds_bpermute_b32 v18, v35, v16
	ds_bpermute_b32 v19, v35, v17
	ds_bpermute_b32 v20, v35, v14
	ds_bpermute_b32 v21, v35, v15
	ds_bpermute_b32 v22, v35, v12
	ds_bpermute_b32 v23, v35, v13
	ds_bpermute_b32 v24, v35, v10
	ds_bpermute_b32 v25, v35, v11
	s_waitcnt lgkmcnt(0)
	v_add_f32_e32 v16, v16, v18
	v_add_f32_e32 v17, v17, v19
	v_add_f32_e32 v14, v14, v20
	v_add_f32_e32 v15, v15, v21
	v_add_f32_e32 v12, v12, v22
	v_add_f32_e32 v13, v13, v23
	v_add_f32_e32 v10, v10, v24
	v_add_f32_e32 v11, v11, v25
	ds_bpermute_b32 v26, v35, v8
	ds_bpermute_b32 v27, v35, v9
	ds_bpermute_b32 v28, v35, v6
	ds_bpermute_b32 v29, v35, v7
	ds_bpermute_b32 v30, v35, v4
	ds_bpermute_b32 v31, v35, v5
	ds_bpermute_b32 v32, v35, v2
	ds_bpermute_b32 v33, v35, v3
	s_waitcnt lgkmcnt(0)
	v_add_f32_e32 v8, v8, v26
	v_add_f32_e32 v9, v9, v27
	v_add_f32_e32 v6, v6, v28
	v_add_f32_e32 v7, v7, v29
	v_add_f32_e32 v4, v4, v30
	v_add_f32_e32 v5, v5, v31
	v_add_f32_e32 v2, v2, v32
	v_add_f32_e32 v3, v3, v33
	s_and_saveexec_b64 s[8:9], vcc
	v_mov_b32_e32 v36, 0
	global_store_dword v36, v16, s[0:1]
	global_store_dword v36, v17, s[0:1] offset:4
	global_store_dword v36, v14, s[0:1] offset:8
	global_store_dword v36, v15, s[0:1] offset:12
	global_store_dword v36, v12, s[0:1] offset:16
	global_store_dword v36, v13, s[0:1] offset:20
	global_store_dword v36, v10, s[0:1] offset:24
	global_store_dword v36, v11, s[0:1] offset:28
	global_store_dword v36, v8, s[0:1] offset:32
	global_store_dword v36, v9, s[0:1] offset:36
	global_store_dword v36, v6, s[0:1] offset:40
	global_store_dword v36, v7, s[0:1] offset:44
	global_store_dword v36, v4, s[0:1] offset:48
	global_store_dword v36, v5, s[0:1] offset:52
	global_store_dword v36, v2, s[0:1] offset:56
	global_store_dword v36, v3, s[0:1] offset:60

.LBB0_1475:
	s_or_b64 exec, exec, s[12:13]
	s_load_dwordx2 s[0:1], s[10:11], 0x1b8
	v_cmp_eq_u32_e32 vcc, 0, v52
	v_lshlrev_b32_e32 v34, 2, v144
	v_xor_b32_e32 v35, 0x4, v34
	ds_bpermute_b32 v18, v35, v14
	ds_bpermute_b32 v19, v35, v15
	ds_bpermute_b32 v20, v35, v12
	ds_bpermute_b32 v21, v35, v13
	ds_bpermute_b32 v22, v35, v10
	ds_bpermute_b32 v23, v35, v11
	ds_bpermute_b32 v24, v35, v8
	ds_bpermute_b32 v25, v35, v9
	s_waitcnt lgkmcnt(0)
	v_add_f32_e32 v14, v14, v18
	v_add_f32_e32 v15, v15, v19
	v_add_f32_e32 v12, v12, v20
	v_add_f32_e32 v13, v13, v21
	v_add_f32_e32 v10, v10, v22
	v_add_f32_e32 v11, v11, v23
	v_add_f32_e32 v8, v8, v24
	v_add_f32_e32 v9, v9, v25
	ds_bpermute_b32 v26, v35, v6
	ds_bpermute_b32 v27, v35, v7
	ds_bpermute_b32 v28, v35, v4
	ds_bpermute_b32 v29, v35, v5
	ds_bpermute_b32 v30, v35, v2
	ds_bpermute_b32 v31, v35, v3
	ds_bpermute_b32 v32, v35, v0
	ds_bpermute_b32 v33, v35, v1
	s_waitcnt lgkmcnt(0)
	v_add_f32_e32 v6, v6, v26
	v_add_f32_e32 v7, v7, v27
	v_add_f32_e32 v4, v4, v28
	v_add_f32_e32 v5, v5, v29
	v_add_f32_e32 v2, v2, v30
	v_add_f32_e32 v3, v3, v31
	v_add_f32_e32 v0, v0, v32
	v_add_f32_e32 v1, v1, v33
	v_xor_b32_e32 v35, 0x8, v34
	ds_bpermute_b32 v18, v35, v14
	ds_bpermute_b32 v19, v35, v15
	ds_bpermute_b32 v20, v35, v12
	ds_bpermute_b32 v21, v35, v13
	ds_bpermute_b32 v22, v35, v10
	ds_bpermute_b32 v23, v35, v11
	ds_bpermute_b32 v24, v35, v8
	ds_bpermute_b32 v25, v35, v9
	s_waitcnt lgkmcnt(0)
	v_add_f32_e32 v14, v14, v18
	v_add_f32_e32 v15, v15, v19
	v_add_f32_e32 v12, v12, v20
	v_add_f32_e32 v13, v13, v21
	v_add_f32_e32 v10, v10, v22
	v_add_f32_e32 v11, v11, v23
	v_add_f32_e32 v8, v8, v24
	v_add_f32_e32 v9, v9, v25
	ds_bpermute_b32 v26, v35, v6
	ds_bpermute_b32 v27, v35, v7
	ds_bpermute_b32 v28, v35, v4
	ds_bpermute_b32 v29, v35, v5
	ds_bpermute_b32 v30, v35, v2
	ds_bpermute_b32 v31, v35, v3
	ds_bpermute_b32 v32, v35, v0
	ds_bpermute_b32 v33, v35, v1
	s_waitcnt lgkmcnt(0)
	v_add_f32_e32 v6, v6, v26
	v_add_f32_e32 v7, v7, v27
	v_add_f32_e32 v4, v4, v28
	v_add_f32_e32 v5, v5, v29
	v_add_f32_e32 v2, v2, v30
	v_add_f32_e32 v3, v3, v31
	v_add_f32_e32 v0, v0, v32
	v_add_f32_e32 v1, v1, v33
	v_xor_b32_e32 v35, 0x10, v34
	ds_bpermute_b32 v18, v35, v14
	ds_bpermute_b32 v19, v35, v15
	ds_bpermute_b32 v20, v35, v12
	ds_bpermute_b32 v21, v35, v13
	ds_bpermute_b32 v22, v35, v10
	ds_bpermute_b32 v23, v35, v11
	ds_bpermute_b32 v24, v35, v8
	ds_bpermute_b32 v25, v35, v9
	s_waitcnt lgkmcnt(0)
	v_add_f32_e32 v14, v14, v18
	v_add_f32_e32 v15, v15, v19
	v_add_f32_e32 v12, v12, v20
	v_add_f32_e32 v13, v13, v21
	v_add_f32_e32 v10, v10, v22
	v_add_f32_e32 v11, v11, v23
	v_add_f32_e32 v8, v8, v24
	v_add_f32_e32 v9, v9, v25
	ds_bpermute_b32 v26, v35, v6
	ds_bpermute_b32 v27, v35, v7
	ds_bpermute_b32 v28, v35, v4
	ds_bpermute_b32 v29, v35, v5
	ds_bpermute_b32 v30, v35, v2
	ds_bpermute_b32 v31, v35, v3
	ds_bpermute_b32 v32, v35, v0
	ds_bpermute_b32 v33, v35, v1
	s_waitcnt lgkmcnt(0)
	v_add_f32_e32 v6, v6, v26
	v_add_f32_e32 v7, v7, v27
	v_add_f32_e32 v4, v4, v28
	v_add_f32_e32 v5, v5, v29
	v_add_f32_e32 v2, v2, v30
	v_add_f32_e32 v3, v3, v31
	v_add_f32_e32 v0, v0, v32
	v_add_f32_e32 v1, v1, v33
	v_xor_b32_e32 v35, 0x20, v34
	ds_bpermute_b32 v18, v35, v14
	ds_bpermute_b32 v19, v35, v15
	ds_bpermute_b32 v20, v35, v12
	ds_bpermute_b32 v21, v35, v13
	ds_bpermute_b32 v22, v35, v10
	ds_bpermute_b32 v23, v35, v11
	ds_bpermute_b32 v24, v35, v8
	ds_bpermute_b32 v25, v35, v9
	s_waitcnt lgkmcnt(0)
	v_add_f32_e32 v14, v14, v18
	v_add_f32_e32 v15, v15, v19
	v_add_f32_e32 v12, v12, v20
	v_add_f32_e32 v13, v13, v21
	v_add_f32_e32 v10, v10, v22
	v_add_f32_e32 v11, v11, v23
	v_add_f32_e32 v8, v8, v24
	v_add_f32_e32 v9, v9, v25
	ds_bpermute_b32 v26, v35, v6
	ds_bpermute_b32 v27, v35, v7
	ds_bpermute_b32 v28, v35, v4
	ds_bpermute_b32 v29, v35, v5
	ds_bpermute_b32 v30, v35, v2
	ds_bpermute_b32 v31, v35, v3
	ds_bpermute_b32 v32, v35, v0
	ds_bpermute_b32 v33, v35, v1
	s_waitcnt lgkmcnt(0)
	v_add_f32_e32 v6, v6, v26
	v_add_f32_e32 v7, v7, v27
	v_add_f32_e32 v4, v4, v28
	v_add_f32_e32 v5, v5, v29
	v_add_f32_e32 v2, v2, v30
	v_add_f32_e32 v3, v3, v31
	v_add_f32_e32 v0, v0, v32
	v_add_f32_e32 v1, v1, v33
	v_xor_b32_e32 v35, 0x40, v34
	ds_bpermute_b32 v18, v35, v14
	ds_bpermute_b32 v19, v35, v15
	ds_bpermute_b32 v20, v35, v12
	ds_bpermute_b32 v21, v35, v13
	ds_bpermute_b32 v22, v35, v10
	ds_bpermute_b32 v23, v35, v11
	ds_bpermute_b32 v24, v35, v8
	ds_bpermute_b32 v25, v35, v9
	s_waitcnt lgkmcnt(0)
	v_add_f32_e32 v14, v14, v18
	v_add_f32_e32 v15, v15, v19
	v_add_f32_e32 v12, v12, v20
	v_add_f32_e32 v13, v13, v21
	v_add_f32_e32 v10, v10, v22
	v_add_f32_e32 v11, v11, v23
	v_add_f32_e32 v8, v8, v24
	v_add_f32_e32 v9, v9, v25
	ds_bpermute_b32 v26, v35, v6
	ds_bpermute_b32 v27, v35, v7
	ds_bpermute_b32 v28, v35, v4
	ds_bpermute_b32 v29, v35, v5
	ds_bpermute_b32 v30, v35, v2
	ds_bpermute_b32 v31, v35, v3
	ds_bpermute_b32 v32, v35, v0
	ds_bpermute_b32 v33, v35, v1
	s_waitcnt lgkmcnt(0)
	v_add_f32_e32 v6, v6, v26
	v_add_f32_e32 v7, v7, v27
	v_add_f32_e32 v4, v4, v28
	v_add_f32_e32 v5, v5, v29
	v_add_f32_e32 v2, v2, v30
	v_add_f32_e32 v3, v3, v31
	v_add_f32_e32 v0, v0, v32
	v_add_f32_e32 v1, v1, v33
	v_xor_b32_e32 v35, 0x80, v34
	ds_bpermute_b32 v18, v35, v14
	ds_bpermute_b32 v19, v35, v15
	ds_bpermute_b32 v20, v35, v12
	ds_bpermute_b32 v21, v35, v13
	ds_bpermute_b32 v22, v35, v10
	ds_bpermute_b32 v23, v35, v11
	ds_bpermute_b32 v24, v35, v8
	ds_bpermute_b32 v25, v35, v9
	s_waitcnt lgkmcnt(0)
	v_add_f32_e32 v14, v14, v18
	v_add_f32_e32 v15, v15, v19
	v_add_f32_e32 v12, v12, v20
	v_add_f32_e32 v13, v13, v21
	v_add_f32_e32 v10, v10, v22
	v_add_f32_e32 v11, v11, v23
	v_add_f32_e32 v8, v8, v24
	v_add_f32_e32 v9, v9, v25
	ds_bpermute_b32 v26, v35, v6
	ds_bpermute_b32 v27, v35, v7
	ds_bpermute_b32 v28, v35, v4
	ds_bpermute_b32 v29, v35, v5
	ds_bpermute_b32 v30, v35, v2
	ds_bpermute_b32 v31, v35, v3
	ds_bpermute_b32 v32, v35, v0
	ds_bpermute_b32 v33, v35, v1
	s_waitcnt lgkmcnt(0)
	v_add_f32_e32 v6, v6, v26
	v_add_f32_e32 v7, v7, v27
	v_add_f32_e32 v4, v4, v28
	v_add_f32_e32 v5, v5, v29
	v_add_f32_e32 v2, v2, v30
	v_add_f32_e32 v3, v3, v31
	v_add_f32_e32 v0, v0, v32
	v_add_f32_e32 v1, v1, v33
	s_and_saveexec_b64 s[12:13], vcc
	v_mov_b32_e32 v36, 0
	global_store_dword v36, v14, s[0:1] offset:64
	global_store_dword v36, v15, s[0:1] offset:68
	global_store_dword v36, v12, s[0:1] offset:72
	global_store_dword v36, v13, s[0:1] offset:76
	global_store_dword v36, v10, s[0:1] offset:80
	global_store_dword v36, v11, s[0:1] offset:84
	global_store_dword v36, v8, s[0:1] offset:88
	global_store_dword v36, v9, s[0:1] offset:92
	global_store_dword v36, v6, s[0:1] offset:96
	global_store_dword v36, v7, s[0:1] offset:100
	global_store_dword v36, v4, s[0:1] offset:104
	global_store_dword v36, v5, s[0:1] offset:108
	global_store_dword v36, v2, s[0:1] offset:112
	global_store_dword v36, v3, s[0:1] offset:116
	global_store_dword v36, v0, s[0:1] offset:120
	global_store_dword v36, v1, s[0:1] offset:124
